# v30 + dense SwiGLU-up GEMM: LDS image in 8-row x 128-byte pieces (full cache lines per LDS-DMA instruction), XOR-swizzled fragment reads
# speedup vs baseline: 1.0000x; 1.0000x over previous
.LBB0_564:
	v_and_b32_e32 v253, 63, v0
	v_lshrrev_b32_e32 v252, 6, v0
	v_lshrrev_b32_e32 v245, 3, v253
	v_and_b32_e32 v251, 7, v253
	v_and_b32_e32 v246, 6, v245
	v_xor_b32_e32 v251, v251, v246
	v_lshlrev_b32_e32 v251, 4, v251
	v_lshl_add_u32 v247, v252, 3, v245
	v_add_u32_e32 v136, 0, v247
	v_lshl_add_u32 v136, v136, 12, v251
	v_add_u32_e32 v132, 64, v247
	v_lshl_add_u32 v132, v132, 12, v251
	v_mov_b32_e32 v138, v136
	v_mov_b32_e32 v140, v132
	v_and_b32_e32 v248, 31, v247
	v_bfe_u32 v249, v248, 2, 2
	v_lshlrev_b32_e32 v249, 3, v249
	v_bfe_u32 v250, v248, 4, 1
	v_lshl_add_u32 v249, v250, 2, v249
	v_and_b32_e32 v250, 3, v248
	v_add_u32_e32 v249, v249, v250
	v_add_u32_e32 v134, 0, v247
	v_and_b32_e32 v134, 0xffffffe0, v134
	v_add_u32_e32 v134, v134, v249
	v_lshl_add_u32 v134, v134, 12, v251
	v_add_u32_e32 v130, 64, v247
	v_and_b32_e32 v130, 0xffffffe0, v130
	v_add_u32_e32 v130, v130, v249
	v_lshl_add_u32 v130, v130, 12, v251
	v_and_b32_e32 v245, 15, v253
	v_lshrrev_b32_e32 v246, 4, v253
	v_and_b32_e32 v247, 6, v245
	v_xor_b32_e32 v246, v246, v247
	v_lshlrev_b32_e32 v246, 4, v246
	v_bfe_u32 v247, v245, 3, 1
	v_lshl_add_u32 v246, v247, 10, v246
	v_and_b32_e32 v247, 7, v245
	v_lshl_add_u32 v246, v247, 7, v246
	v_lshrrev_b32_e32 v247, 2, v252
	v_lshl_add_u32 v154, v247, 13, v246
	v_and_b32_e32 v247, 3, v252
	v_lshl_add_u32 v150, v247, 12, v246
	s_cmp_lt_i32 s90, 8
	s_cselect_b64 s[0:1], -1, 0
	s_cmp_gt_i32 s91, 7
	s_cselect_b64 s[2:3], -1, 0
	s_and_b64 s[0:1], s[0:1], s[2:3]
	s_andn2_b64 vcc, exec, s[0:1]
	s_cbranch_vccnz .LBB0_581
	s_cmpk_gt_i32 s87, 0xabf
	v_readfirstlane_b32 s5, v0
	s_cbranch_scc1 .LBB0_581
	v_lshrrev_b32_e32 v1, 5, v0
	s_waitcnt lgkmcnt(0)
	v_lshrrev_b32_e32 v3, 1, v0
	v_and_b32_e32 v1, 4, v1
	v_bfe_u32 v2, v0, 2, 2
	s_waitcnt vmcnt(6)
	v_and_b32_e32 v13, 24, v3
	s_add_u32 s28, s58, 0x59680000
	v_or3_b32 v1, v1, v2, v13
	v_lshlrev_b32_e32 v2, 4, v0
	s_addc_u32 s29, s59, 0
	v_or_b32_e32 v10, 0x2000, v2
	s_add_u32 s30, s58, 0x2200000
	v_lshrrev_b32_e32 v3, 7, v10
	s_movk_i32 s2, 0x60
	s_addc_u32 s31, s59, 0
	v_and_or_b32 v4, v3, s2, v1
	s_waitcnt vmcnt(5)
	v_bfe_u32 v14, v0, 2, 4
	s_movk_i32 s2, 0x70
	s_ashr_i32 s34, s87, 31
	v_and_or_b32 v3, v3, s2, v14
	s_lshr_b32 s2, s34, 29
	s_add_i32 s2, s87, s2
	s_lshr_b32 s8, s5, 6
	s_ashr_i32 s3, s2, 3
	s_and_b32 s2, s2, -8
	s_lshr_b32 s10, s5, 8
	s_lshl_b32 s33, s8, 10
	s_sub_i32 s2, s87, s2
	s_cmp_lt_i32 s2, 0
	s_movk_i32 s35, 0x159
	s_cselect_b32 s4, s35, 0x158
	s_mul_i32 s2, s2, s4
	s_add_i32 s2, s2, s3
	s_mul_hi_i32 s3, s2, 0x2fa0be83
	s_lshr_b32 s4, s3, 31
	s_ashr_i32 s3, s3, 5
	s_add_i32 s3, s3, s4
	s_lshl_b32 s6, s3, 2
	s_mulk_i32 s3, 0xac
	s_sub_i32 s2, s2, s3
	s_bfe_u32 s3, s2, 0x2001d
	s_add_i32 s3, s2, s3
	s_sext_i32_i16 s4, s3
	s_and_b32 s3, s3, 0xfffc
	s_sub_i32 s2, s2, s3
	s_sext_i32_i16 s2, s2
	v_and_b32_e32 v5, 32, v0
	s_lshr_b32 s4, s4, 2
	s_add_i32 s20, s6, s2
	v_bitop3_b32 v11, v2, v5, 48 bitop3:0x6c
	v_and_b32_e32 v12, 64, v0
	s_ashr_i32 s21, s20, 31
	s_bfe_i64 s[6:7], s[4:5], 0x100000
	v_or_b32_e32 v2, v11, v12
	s_lshl_b64 s[2:3], s[20:21], 20
	s_lshl_b64 s[6:7], s[6:7], 20
	v_lshrrev_b32_e32 v3, 3, v0
	s_add_u32 s24, s30, s6
	v_and_or_b32 v1, v3, 32, v1
	s_addc_u32 s25, s31, s7
	s_add_i32 s21, s33, 0
	s_add_i32 m0, s21, 0x10000
	global_load_lds_dwordx4 v134, s[24:25]
	s_add_i32 m0, s21, 0x12000
	s_add_u32 s6, s24, 0x80000
	global_load_lds_dwordx4 v130, s[24:25]
	s_addc_u32 s7, s25, 0
	s_add_i32 m0, s21, 0x14000
	v_and_or_b32 v1, v3, 48, v14
	global_load_lds_dwordx4 v134, s[6:7]
	s_add_i32 m0, s21, 0x16000
	s_add_u32 s22, s28, s2
	s_addc_u32 s23, s29, s3
	s_add_i32 s36, s21, 0x2000
	global_load_lds_dwordx4 v130, s[6:7]
	s_mov_b32 m0, s21
	s_add_u32 s2, s22, 0x80000
	global_load_lds_dwordx4 v136, s[22:23]
	s_mov_b32 m0, s36
	s_addc_u32 s3, s23, 0
	s_add_i32 s37, s21, 0x4000
	global_load_lds_dwordx4 v132, s[22:23]
	s_mov_b32 m0, s37
	s_add_i32 s42, s21, 0x6000
	global_load_lds_dwordx4 v136, s[2:3]
	s_mov_b32 m0, s42
	v_mov_b32_e32 v135, 0
	global_load_lds_dwordx4 v132, s[2:3]
	v_mov_b32_e32 v131, v135
	v_mov_b32_e32 v137, v135
	v_mov_b32_e32 v133, v135
	s_cmp_eq_u32 s10, 1
	s_mov_b32 s43, 0
	v_lshl_add_u64 v[8:9], s[24:25], 0, v[134:135]
	v_lshl_add_u64 v[6:7], s[24:25], 0, v[130:131]
	v_lshl_add_u64 v[2:3], s[22:23], 0, v[136:137]
	s_cselect_b64 s[2:3], -1, 0
	s_cmp_lg_u32 s10, 1
	v_lshl_add_u64 v[4:5], s[22:23], 0, v[132:133]
	s_cbranch_scc1 .LBB0_568
	s_barrier
.LBB0_568:
	s_add_u32 s6, s58, 0x65680000
	s_addc_u32 s7, s59, 0
	s_lshl_b32 s8, s8, 5
	s_and_b32 s14, s8, 0x60
	s_mov_b64 s[8:9], 0x80
	s_add_i32 m0, s21, 0x18000
	v_lshl_add_u64 v[8:9], v[8:9], 0, s[8:9]
	s_lshl_b32 s11, s10, 13
	s_lshl_b32 s15, s14, 7
	s_waitcnt vmcnt(2)
	s_barrier
	global_load_lds_dwordx4 v[8:9], off
	v_lshl_add_u64 v[6:7], v[6:7], 0, s[8:9]
	s_add_i32 m0, s21, 0x1a000
	s_add_i32 s44, s21, 0x8000
	s_add_i32 s45, s21, 0xa000
	global_load_lds_dwordx4 v[6:7], off
	v_lshl_add_u64 v[2:3], v[2:3], 0, s[8:9]
	s_mov_b32 m0, s44
	s_add_u32 s12, s24, 0x80080
	global_load_lds_dwordx4 v[2:3], off
	v_lshl_add_u64 v[2:3], v[4:5], 0, s[8:9]
	s_mov_b32 m0, s45
	s_addc_u32 s13, s25, 0
	global_load_lds_dwordx4 v[2:3], off
	s_add_i32 m0, s21, 0x1c000
	v_lshl_add_u64 v[2:3], s[12:13], 0, v[134:135]
	global_load_lds_dwordx4 v[2:3], off
	v_lshl_add_u64 v[2:3], s[12:13], 0, v[130:131]
	s_add_i32 m0, s21, 0x1e000
	s_sext_i32_i16 s64, s4
	global_load_lds_dwordx4 v[2:3], off
	v_and_b32_e32 v2, 15, v0
	v_lshlrev_b32_e32 v3, 1, v13
	v_lshlrev_b32_e32 v5, 6, v0
	s_movk_i32 s4, 0x3c0
	v_lshl_or_b32 v1, s10, 6, v2
	v_lshl_or_b32 v2, v2, 6, v3
	v_and_b32_e32 v4, 32, v244
	v_and_or_b32 v3, v5, s4, v3
	v_lshlrev_b32_e32 v3, 9, v0
	v_bitop3_b32 v2, v2, s11, v4 bitop3:0xde
	v_and_b32_e32 v3, 0x30000, v3
	v_lshlrev_b32_e32 v4, 12, v14
	v_or3_b32 v3, v11, v3, v4
	v_lshlrev_b32_e32 v3, 5, v10
	s_waitcnt vmcnt(6)
	s_cmpk_lt_u32 s5, 0x100
	v_and_b32_e32 v3, 0x70000, v3
	s_cselect_b64 s[10:11], -1, 0
	v_or3_b32 v3, v11, v3, v4
	s_add_i32 s61, 0, 0x10000
	s_add_i32 s62, 0, 0x14000
	s_ashr_i32 s60, s96, 31
	v_or_b32_e32 v151, s14, v13
	v_mov_b32_e32 v139, v135
	v_mov_b32_e32 v141, v135
	v_mov_b64_e32 v[142:143], 0xac0
	v_mov_b64_e32 v[144:145], 0xabf
	v_add_u32_e32 v152, s61, v150
	v_add_u32_e32 v153, s62, v150
	s_movk_i32 s63, 0x2b00
	s_barrier
	s_waitcnt vmcnt(0)
	v_xor_b32_e32 v246, 64, v152
	v_xor_b32_e32 v247, 64, v153
	v_xor_b32_e32 v248, 64, v154
	v_xor_b32_e32 v250, 64, v150
	s_branch .LBB0_571

.LBB0_574:
	ds_read_b128 v[146:149], v152
	ds_read_b128 v[156:159], v246
	ds_read_b128 v[160:163], v152 offset:2048
	ds_read_b128 v[164:167], v246 offset:2048
	ds_read_b128 v[168:171], v153
	ds_read_b128 v[172:175], v247
	ds_read_b128 v[176:179], v153 offset:2048
	ds_read_b128 v[180:183], v247 offset:2048
	s_add_u32 s24, s22, 0xfff80080
	s_addc_u32 s25, s23, -1
	s_cmp_eq_u32 s69, 28
	s_cselect_b32 s27, s15, s25
	s_cselect_b32 s26, s65, s24
	s_cselect_b32 s25, s13, s68
	s_cselect_b32 s24, s66, s67
	s_add_i32 m0, s21, 0xc000
	ds_read_b128 v[184:187], v154
	ds_read_b128 v[188:191], v248
	ds_read_b128 v[192:195], v154 offset:2048
	ds_read_b128 v[196:199], v248 offset:2048
	ds_read_b128 v[200:203], v154 offset:4096
	ds_read_b128 v[204:207], v248 offset:4096
	ds_read_b128 v[208:211], v154 offset:6144
	ds_read_b128 v[212:215], v248 offset:6144
	global_load_lds_dwordx4 v138, s[22:23]
	s_add_i32 m0, s21, 0xe000
	s_nop 0
	global_load_lds_dwordx4 v140, s[22:23]
	s_waitcnt vmcnt(8)
	s_waitcnt lgkmcnt(0)
	s_barrier
	s_setprio 1
	s_waitcnt lgkmcnt(0)
	v_mfma_f32_16x16x32_bf16 v[126:129], v[146:149], v[184:187], v[126:129]
	v_mfma_f32_16x16x32_bf16 v[122:125], v[160:163], v[184:187], v[122:125]
	v_mfma_f32_16x16x32_bf16 v[110:113], v[146:149], v[192:195], v[110:113]
	v_mfma_f32_16x16x32_bf16 v[106:109], v[160:163], v[192:195], v[106:109]
	v_mfma_f32_16x16x32_bf16 v[94:97], v[146:149], v[200:203], v[94:97]
	v_mfma_f32_16x16x32_bf16 v[90:93], v[160:163], v[200:203], v[90:93]
	v_mfma_f32_16x16x32_bf16 v[78:81], v[146:149], v[208:211], v[78:81]
	v_mfma_f32_16x16x32_bf16 v[74:77], v[160:163], v[208:211], v[74:77]
	v_mfma_f32_16x16x32_bf16 v[126:129], v[156:159], v[188:191], v[126:129]
	v_mfma_f32_16x16x32_bf16 v[122:125], v[164:167], v[188:191], v[122:125]
	v_mfma_f32_16x16x32_bf16 v[110:113], v[156:159], v[196:199], v[110:113]
	v_mfma_f32_16x16x32_bf16 v[106:109], v[164:167], v[196:199], v[106:109]
	v_mfma_f32_16x16x32_bf16 v[94:97], v[156:159], v[204:207], v[94:97]
	v_mfma_f32_16x16x32_bf16 v[90:93], v[164:167], v[204:207], v[90:93]
	v_mfma_f32_16x16x32_bf16 v[78:81], v[156:159], v[212:215], v[78:81]
	v_mfma_f32_16x16x32_bf16 v[74:77], v[164:167], v[212:215], v[74:77]
	s_setprio 0
	s_setprio 1
	v_mfma_f32_16x16x32_bf16 v[118:121], v[168:171], v[184:187], v[118:121]
	v_mfma_f32_16x16x32_bf16 v[114:117], v[176:179], v[184:187], v[114:117]
	v_mfma_f32_16x16x32_bf16 v[102:105], v[168:171], v[192:195], v[102:105]
	v_mfma_f32_16x16x32_bf16 v[98:101], v[176:179], v[192:195], v[98:101]
	v_mfma_f32_16x16x32_bf16 v[86:89], v[168:171], v[200:203], v[86:89]
	v_mfma_f32_16x16x32_bf16 v[82:85], v[176:179], v[200:203], v[82:85]
	v_mfma_f32_16x16x32_bf16 v[70:73], v[168:171], v[208:211], v[70:73]
	v_mfma_f32_16x16x32_bf16 v[66:69], v[176:179], v[208:211], v[66:69]
	v_mfma_f32_16x16x32_bf16 v[118:121], v[172:175], v[188:191], v[118:121]
	v_mfma_f32_16x16x32_bf16 v[114:117], v[180:183], v[188:191], v[114:117]
	v_mfma_f32_16x16x32_bf16 v[102:105], v[172:175], v[196:199], v[102:105]
	v_mfma_f32_16x16x32_bf16 v[98:101], v[180:183], v[196:199], v[98:101]
	v_mfma_f32_16x16x32_bf16 v[86:89], v[172:175], v[204:207], v[86:89]
	v_mfma_f32_16x16x32_bf16 v[82:85], v[180:183], v[204:207], v[82:85]
	v_mfma_f32_16x16x32_bf16 v[70:73], v[172:175], v[212:215], v[70:73]
	v_mfma_f32_16x16x32_bf16 v[66:69], v[180:183], v[212:215], v[66:69]
	s_setprio 0
	s_barrier
	s_add_i32 s70, s61, s33
	v_lshl_add_u64 v[216:217], s[24:25], 0, v[134:135]
	s_mov_b32 m0, s70
	ds_read_b128 v[184:187], v154 offset:16384
	ds_read_b128 v[188:191], v248 offset:16384
	ds_read_b128 v[192:195], v154 offset:18432
	ds_read_b128 v[196:199], v248 offset:18432
	ds_read_b128 v[200:203], v154 offset:20480
	ds_read_b128 v[204:207], v248 offset:20480
	ds_read_b128 v[208:211], v154 offset:22528
	ds_read_b128 v[212:215], v248 offset:22528
	global_load_lds_dwordx4 v134, s[24:25]
	s_add_i32 m0, s70, 0x2000
	s_add_u32 s70, s24, 0x80000
	v_lshl_add_u64 v[218:219], s[24:25], 0, v[130:131]
	s_addc_u32 s71, s25, 0
	s_add_i32 s72, s62, s33
	global_load_lds_dwordx4 v130, s[24:25]
	s_mov_b32 m0, s72
	v_lshl_add_u64 v[222:223], s[26:27], 0, v[132:133]
	global_load_lds_dwordx4 v134, s[70:71]
	s_add_i32 m0, s72, 0x2000
	s_nop 0
	global_load_lds_dwordx4 v130, s[70:71]
	v_lshl_add_u64 v[220:221], s[26:27], 0, v[136:137]
	s_mov_b32 m0, s21
	s_nop 0
	global_load_lds_dwordx4 v136, s[26:27]
	s_mov_b32 m0, s36
	s_nop 0
	global_load_lds_dwordx4 v132, s[26:27]
	s_waitcnt vmcnt(8)
	s_waitcnt lgkmcnt(0)
	s_barrier
	s_setprio 1
	s_waitcnt lgkmcnt(0)
	v_mfma_f32_16x16x32_bf16 v[62:65], v[146:149], v[184:187], v[62:65]
	v_mfma_f32_16x16x32_bf16 v[58:61], v[160:163], v[184:187], v[58:61]
	v_mfma_f32_16x16x32_bf16 v[46:49], v[146:149], v[192:195], v[46:49]
	v_mfma_f32_16x16x32_bf16 v[42:45], v[160:163], v[192:195], v[42:45]
	v_mfma_f32_16x16x32_bf16 v[30:33], v[146:149], v[200:203], v[30:33]
	v_mfma_f32_16x16x32_bf16 v[26:29], v[160:163], v[200:203], v[26:29]
	v_mfma_f32_16x16x32_bf16 v[14:17], v[146:149], v[208:211], v[14:17]
	v_mfma_f32_16x16x32_bf16 v[10:13], v[160:163], v[208:211], v[10:13]
	v_mfma_f32_16x16x32_bf16 v[62:65], v[156:159], v[188:191], v[62:65]
	v_mfma_f32_16x16x32_bf16 v[58:61], v[164:167], v[188:191], v[58:61]
	v_mfma_f32_16x16x32_bf16 v[46:49], v[156:159], v[196:199], v[46:49]
	v_mfma_f32_16x16x32_bf16 v[42:45], v[164:167], v[196:199], v[42:45]
	v_mfma_f32_16x16x32_bf16 v[30:33], v[156:159], v[204:207], v[30:33]
	v_mfma_f32_16x16x32_bf16 v[26:29], v[164:167], v[204:207], v[26:29]
	v_mfma_f32_16x16x32_bf16 v[14:17], v[156:159], v[212:215], v[14:17]
	v_mfma_f32_16x16x32_bf16 v[10:13], v[164:167], v[212:215], v[10:13]
	s_setprio 0
	s_setprio 1
	v_mfma_f32_16x16x32_bf16 v[54:57], v[168:171], v[184:187], v[54:57]
	v_mfma_f32_16x16x32_bf16 v[50:53], v[176:179], v[184:187], v[50:53]
	v_mfma_f32_16x16x32_bf16 v[38:41], v[168:171], v[192:195], v[38:41]
	v_mfma_f32_16x16x32_bf16 v[34:37], v[176:179], v[192:195], v[34:37]
	v_mfma_f32_16x16x32_bf16 v[22:25], v[168:171], v[200:203], v[22:25]
	v_mfma_f32_16x16x32_bf16 v[18:21], v[176:179], v[200:203], v[18:21]
	v_mfma_f32_16x16x32_bf16 v[6:9], v[168:171], v[208:211], v[6:9]
	v_mfma_f32_16x16x32_bf16 v[2:5], v[176:179], v[208:211], v[2:5]
	v_mfma_f32_16x16x32_bf16 v[54:57], v[172:175], v[188:191], v[54:57]
	v_mfma_f32_16x16x32_bf16 v[50:53], v[180:183], v[188:191], v[50:53]
	v_mfma_f32_16x16x32_bf16 v[38:41], v[172:175], v[196:199], v[38:41]
	v_mfma_f32_16x16x32_bf16 v[34:37], v[180:183], v[196:199], v[34:37]
	v_mfma_f32_16x16x32_bf16 v[22:25], v[172:175], v[204:207], v[22:25]
	v_mfma_f32_16x16x32_bf16 v[18:21], v[180:183], v[204:207], v[18:21]
	v_mfma_f32_16x16x32_bf16 v[6:9], v[172:175], v[212:215], v[6:9]
	v_mfma_f32_16x16x32_bf16 v[2:5], v[180:183], v[212:215], v[2:5]
	s_setprio 0
	s_barrier
	s_add_i32 s70, 0, 0x18000
	v_add_u32_e32 v155, s70, v150
	v_add_u32_e32 v249, s70, v250
	s_add_i32 s71, 0, 0x1c000
	ds_read_b128 v[146:149], v155
	ds_read_b128 v[156:159], v249
	ds_read_b128 v[160:163], v155 offset:2048
	ds_read_b128 v[164:167], v249 offset:2048
	v_add_u32_e32 v155, s71, v150
	v_add_u32_e32 v249, s71, v250
	ds_read_b128 v[168:171], v155
	ds_read_b128 v[172:175], v249
	ds_read_b128 v[176:179], v155 offset:2048
	ds_read_b128 v[180:183], v249 offset:2048
	s_add_u32 s26, s26, 0x80000
	s_addc_u32 s27, s27, 0
	s_mov_b32 m0, s37
	ds_read_b128 v[184:187], v154 offset:32768
	ds_read_b128 v[188:191], v248 offset:32768
	ds_read_b128 v[192:195], v154 offset:34816
	ds_read_b128 v[196:199], v248 offset:34816
	ds_read_b128 v[200:203], v154 offset:36864
	ds_read_b128 v[204:207], v248 offset:36864
	ds_read_b128 v[208:211], v154 offset:38912
	ds_read_b128 v[212:215], v248 offset:38912
	global_load_lds_dwordx4 v136, s[26:27]
	s_mov_b32 m0, s42
	s_nop 0
	global_load_lds_dwordx4 v132, s[26:27]
	s_waitcnt vmcnt(8)
	s_waitcnt lgkmcnt(0)
	s_barrier
	s_setprio 1
	s_waitcnt lgkmcnt(0)
	v_mfma_f32_16x16x32_bf16 v[126:129], v[146:149], v[184:187], v[126:129]
	v_mfma_f32_16x16x32_bf16 v[122:125], v[160:163], v[184:187], v[122:125]
	v_mfma_f32_16x16x32_bf16 v[110:113], v[146:149], v[192:195], v[110:113]
	v_mfma_f32_16x16x32_bf16 v[106:109], v[160:163], v[192:195], v[106:109]
	v_mfma_f32_16x16x32_bf16 v[94:97], v[146:149], v[200:203], v[94:97]
	v_mfma_f32_16x16x32_bf16 v[90:93], v[160:163], v[200:203], v[90:93]
	v_mfma_f32_16x16x32_bf16 v[78:81], v[146:149], v[208:211], v[78:81]
	v_mfma_f32_16x16x32_bf16 v[74:77], v[160:163], v[208:211], v[74:77]
	v_mfma_f32_16x16x32_bf16 v[126:129], v[156:159], v[188:191], v[126:129]
	v_mfma_f32_16x16x32_bf16 v[122:125], v[164:167], v[188:191], v[122:125]
	v_mfma_f32_16x16x32_bf16 v[110:113], v[156:159], v[196:199], v[110:113]
	v_mfma_f32_16x16x32_bf16 v[106:109], v[164:167], v[196:199], v[106:109]
	v_mfma_f32_16x16x32_bf16 v[94:97], v[156:159], v[204:207], v[94:97]
	v_mfma_f32_16x16x32_bf16 v[90:93], v[164:167], v[204:207], v[90:93]
	v_mfma_f32_16x16x32_bf16 v[78:81], v[156:159], v[212:215], v[78:81]
	v_mfma_f32_16x16x32_bf16 v[74:77], v[164:167], v[212:215], v[74:77]
	s_setprio 0
	s_setprio 1
	v_mfma_f32_16x16x32_bf16 v[118:121], v[168:171], v[184:187], v[118:121]
	v_mfma_f32_16x16x32_bf16 v[114:117], v[176:179], v[184:187], v[114:117]
	v_mfma_f32_16x16x32_bf16 v[102:105], v[168:171], v[192:195], v[102:105]
	v_mfma_f32_16x16x32_bf16 v[98:101], v[176:179], v[192:195], v[98:101]
	v_mfma_f32_16x16x32_bf16 v[86:89], v[168:171], v[200:203], v[86:89]
	v_mfma_f32_16x16x32_bf16 v[82:85], v[176:179], v[200:203], v[82:85]
	v_mfma_f32_16x16x32_bf16 v[70:73], v[168:171], v[208:211], v[70:73]
	v_mfma_f32_16x16x32_bf16 v[66:69], v[176:179], v[208:211], v[66:69]
	v_mfma_f32_16x16x32_bf16 v[118:121], v[172:175], v[188:191], v[118:121]
	v_mfma_f32_16x16x32_bf16 v[114:117], v[180:183], v[188:191], v[114:117]
	v_mfma_f32_16x16x32_bf16 v[102:105], v[172:175], v[196:199], v[102:105]
	v_mfma_f32_16x16x32_bf16 v[98:101], v[180:183], v[196:199], v[98:101]
	v_mfma_f32_16x16x32_bf16 v[86:89], v[172:175], v[204:207], v[86:89]
	v_mfma_f32_16x16x32_bf16 v[82:85], v[180:183], v[204:207], v[82:85]
	v_mfma_f32_16x16x32_bf16 v[70:73], v[172:175], v[212:215], v[70:73]
	v_mfma_f32_16x16x32_bf16 v[66:69], v[180:183], v[212:215], v[66:69]
	s_setprio 0
	s_barrier
	s_add_i32 s26, s70, s33
	v_lshl_add_u64 v[216:217], v[216:217], 0, s[8:9]
	s_mov_b32 m0, s26
	ds_read_b128 v[184:187], v154 offset:49152
	ds_read_b128 v[188:191], v248 offset:49152
	ds_read_b128 v[192:195], v154 offset:51200
	ds_read_b128 v[196:199], v248 offset:51200
	ds_read_b128 v[200:203], v154 offset:53248
	ds_read_b128 v[204:207], v248 offset:53248
	ds_read_b128 v[208:211], v154 offset:55296
	ds_read_b128 v[212:215], v248 offset:55296
	global_load_lds_dwordx4 v[216:217], off
	s_add_i32 m0, s26, 0x2000
	s_add_u32 s24, s24, 0x80080
	v_lshl_add_u64 v[216:217], v[218:219], 0, s[8:9]
	s_addc_u32 s25, s25, 0
	s_add_i32 s26, s71, s33
	global_load_lds_dwordx4 v[216:217], off
	s_mov_b32 m0, s26
	s_nop 0
	global_load_lds_dwordx4 v134, s[24:25]
	s_add_i32 m0, s26, 0x2000
	s_nop 0
	global_load_lds_dwordx4 v130, s[24:25]
	v_lshl_add_u64 v[216:217], v[220:221], 0, s[8:9]
	s_mov_b32 m0, s44
	s_nop 0
	global_load_lds_dwordx4 v[216:217], off
	v_lshl_add_u64 v[216:217], v[222:223], 0, s[8:9]
	s_mov_b32 m0, s45
	s_nop 0
	global_load_lds_dwordx4 v[216:217], off
	s_waitcnt vmcnt(8)
	s_waitcnt lgkmcnt(0)
	s_barrier
	s_setprio 1
	s_waitcnt lgkmcnt(0)
	v_mfma_f32_16x16x32_bf16 v[62:65], v[146:149], v[184:187], v[62:65]
	v_mfma_f32_16x16x32_bf16 v[58:61], v[160:163], v[184:187], v[58:61]
	v_mfma_f32_16x16x32_bf16 v[46:49], v[146:149], v[192:195], v[46:49]
	v_mfma_f32_16x16x32_bf16 v[42:45], v[160:163], v[192:195], v[42:45]
	v_mfma_f32_16x16x32_bf16 v[30:33], v[146:149], v[200:203], v[30:33]
	v_mfma_f32_16x16x32_bf16 v[26:29], v[160:163], v[200:203], v[26:29]
	v_mfma_f32_16x16x32_bf16 v[14:17], v[146:149], v[208:211], v[14:17]
	v_mfma_f32_16x16x32_bf16 v[10:13], v[160:163], v[208:211], v[10:13]
	v_mfma_f32_16x16x32_bf16 v[62:65], v[156:159], v[188:191], v[62:65]
	v_mfma_f32_16x16x32_bf16 v[58:61], v[164:167], v[188:191], v[58:61]
	v_mfma_f32_16x16x32_bf16 v[46:49], v[156:159], v[196:199], v[46:49]
	v_mfma_f32_16x16x32_bf16 v[42:45], v[164:167], v[196:199], v[42:45]
	v_mfma_f32_16x16x32_bf16 v[30:33], v[156:159], v[204:207], v[30:33]
	v_mfma_f32_16x16x32_bf16 v[26:29], v[164:167], v[204:207], v[26:29]
	v_mfma_f32_16x16x32_bf16 v[14:17], v[156:159], v[212:215], v[14:17]
	v_mfma_f32_16x16x32_bf16 v[10:13], v[164:167], v[212:215], v[10:13]
	s_setprio 0
	s_setprio 1
	v_mfma_f32_16x16x32_bf16 v[54:57], v[168:171], v[184:187], v[54:57]
	v_mfma_f32_16x16x32_bf16 v[50:53], v[176:179], v[184:187], v[50:53]
	v_mfma_f32_16x16x32_bf16 v[38:41], v[168:171], v[192:195], v[38:41]
	v_mfma_f32_16x16x32_bf16 v[34:37], v[176:179], v[192:195], v[34:37]
	v_mfma_f32_16x16x32_bf16 v[22:25], v[168:171], v[200:203], v[22:25]
	v_mfma_f32_16x16x32_bf16 v[18:21], v[176:179], v[200:203], v[18:21]
	v_mfma_f32_16x16x32_bf16 v[6:9], v[168:171], v[208:211], v[6:9]
	v_mfma_f32_16x16x32_bf16 v[2:5], v[176:179], v[208:211], v[2:5]
	v_mfma_f32_16x16x32_bf16 v[54:57], v[172:175], v[188:191], v[54:57]
	v_mfma_f32_16x16x32_bf16 v[50:53], v[180:183], v[188:191], v[50:53]
	v_mfma_f32_16x16x32_bf16 v[38:41], v[172:175], v[196:199], v[38:41]
	v_mfma_f32_16x16x32_bf16 v[34:37], v[180:183], v[196:199], v[34:37]
	v_mfma_f32_16x16x32_bf16 v[22:25], v[172:175], v[204:207], v[22:25]
	v_mfma_f32_16x16x32_bf16 v[18:21], v[180:183], v[204:207], v[18:21]
	v_mfma_f32_16x16x32_bf16 v[6:9], v[172:175], v[212:215], v[6:9]
	v_mfma_f32_16x16x32_bf16 v[2:5], v[180:183], v[212:215], v[2:5]
	s_setprio 0
	s_barrier
	s_add_i32 s69, s69, 2
	s_add_u32 s22, s22, 0x100
	s_addc_u32 s23, s23, 0
	s_add_u32 s67, s67, 0x100
	s_addc_u32 s68, s68, 0
	s_cmp_gt_u32 s69, 29
	s_cbranch_scc0 .LBB0_574
	s_and_b64 vcc, exec, s[10:11]
	s_cbranch_vccz .LBB0_577
	s_barrier

.LBB0_1257:
	ds_read_b128 v[20:23], v202
	ds_read_b128 v[166:169], v202 offset:1024
	ds_read_b128 v[14:17], v202 offset:2048
	ds_read_b128 v[162:165], v202 offset:3072
	ds_read_b128 v[8:11], v203
	ds_read_b128 v[158:161], v203 offset:1024
	ds_read_b128 v[2:5], v203 offset:2048
	ds_read_b128 v[154:157], v203 offset:3072
	s_add_u32 s22, s20, 0xfffc0080
	s_addc_u32 s23, s21, -1
	s_cmp_eq_u32 s63, 12
	s_cselect_b32 s25, s11, s23
	s_cselect_b32 s24, s49, s22
	s_cselect_b32 s23, s13, s62
	s_cselect_b32 s22, s60, s61
	s_add_i32 m0, s35, 0xc000
	ds_read_b128 v[184:187], v204
	ds_read_b128 v[188:191], v204 offset:1024
	ds_read_b128 v[206:209], v204 offset:2048
	ds_read_b128 v[222:225], v204 offset:3072
	ds_read_b128 v[212:215], v204 offset:4096
	ds_read_b128 v[226:229], v204 offset:5120
	ds_read_b128 v[218:221], v204 offset:6144
	ds_read_b128 v[230:233], v204 offset:7168
	global_load_lds_dwordx4 v180, s[20:21]
	s_add_i32 m0, s35, 0xe000
	s_nop 0
	global_load_lds_dwordx4 v182, s[20:21]
	s_waitcnt vmcnt(8)
	s_waitcnt lgkmcnt(0)
	s_barrier
	s_setprio 1
	s_waitcnt lgkmcnt(0)
	v_mov_b32_e32 v24, v166
	v_mov_b32_e32 v25, v167
	s_nop 1
	v_mfma_scale_f32_16x16x128_f8f6f4 v[150:153], v[20:25], v[184:189], v[150:153], v168, v190 op_sel_hi:[0,0,0] cbsz:2 blgp:2
	v_mov_b32_e32 v18, v162
	v_mov_b32_e32 v19, v163
	s_nop 1
	v_mfma_scale_f32_16x16x128_f8f6f4 v[138:141], v[14:19], v[184:189], v[138:141], v164, v190 op_sel_hi:[0,0,0] cbsz:2 blgp:2
	v_mov_b32_e32 v210, v222
	v_mov_b32_e32 v211, v223
	s_nop 1
	v_mfma_scale_f32_16x16x128_f8f6f4 v[134:137], v[20:25], v[206:211], v[134:137], v168, v224 op_sel_hi:[0,0,0] cbsz:2 blgp:2
	v_mfma_scale_f32_16x16x128_f8f6f4 v[122:125], v[14:19], v[206:211], v[122:125], v164, v224 op_sel_hi:[0,0,0] cbsz:2 blgp:2
	v_mov_b32_e32 v216, v226
	v_mov_b32_e32 v217, v227
	s_nop 1
	v_mfma_scale_f32_16x16x128_f8f6f4 v[118:121], v[20:25], v[212:217], v[118:121], v168, v228 op_sel_hi:[0,0,0] cbsz:2 blgp:2
	v_mfma_scale_f32_16x16x128_f8f6f4 v[106:109], v[14:19], v[212:217], v[106:109], v164, v228 op_sel_hi:[0,0,0] cbsz:2 blgp:2
	v_mov_b32_e32 v222, v230
	v_mov_b32_e32 v223, v231
	s_nop 1
	v_mfma_scale_f32_16x16x128_f8f6f4 v[102:105], v[20:25], v[218:223], v[102:105], v168, v232 op_sel_hi:[0,0,0] cbsz:2 blgp:2
	v_mfma_scale_f32_16x16x128_f8f6f4 v[90:93], v[14:19], v[218:223], v[90:93], v164, v232 op_sel_hi:[0,0,0] cbsz:2 blgp:2
	s_setprio 0
	s_setprio 1
	v_mov_b32_e32 v12, v158
	v_mov_b32_e32 v13, v159
	s_nop 1
	v_mfma_scale_f32_16x16x128_f8f6f4 v[146:149], v[8:13], v[184:189], v[146:149], v160, v190 op_sel_hi:[0,0,0] cbsz:2 blgp:2
	v_mov_b32_e32 v6, v154
	v_mov_b32_e32 v7, v155
	s_nop 1
	v_mfma_scale_f32_16x16x128_f8f6f4 v[142:145], v[2:7], v[184:189], v[142:145], v156, v190 op_sel_hi:[0,0,0] cbsz:2 blgp:2
	v_mfma_scale_f32_16x16x128_f8f6f4 v[130:133], v[8:13], v[206:211], v[130:133], v160, v224 op_sel_hi:[0,0,0] cbsz:2 blgp:2
	v_mfma_scale_f32_16x16x128_f8f6f4 v[126:129], v[2:7], v[206:211], v[126:129], v156, v224 op_sel_hi:[0,0,0] cbsz:2 blgp:2
	v_mfma_scale_f32_16x16x128_f8f6f4 v[114:117], v[8:13], v[212:217], v[114:117], v160, v228 op_sel_hi:[0,0,0] cbsz:2 blgp:2
	v_mfma_scale_f32_16x16x128_f8f6f4 v[110:113], v[2:7], v[212:217], v[110:113], v156, v228 op_sel_hi:[0,0,0] cbsz:2 blgp:2
	v_mfma_scale_f32_16x16x128_f8f6f4 v[98:101], v[8:13], v[218:223], v[98:101], v160, v232 op_sel_hi:[0,0,0] cbsz:2 blgp:2
	v_mfma_scale_f32_16x16x128_f8f6f4 v[94:97], v[2:7], v[218:223], v[94:97], v156, v232 op_sel_hi:[0,0,0] cbsz:2 blgp:2
	s_setprio 0
	s_barrier
	s_add_i32 s64, s42, s27
	v_lshl_add_u64 v[184:185], s[22:23], 0, v[172:173]
	s_mov_b32 m0, s64
	ds_read_b128 v[206:209], v204 offset:16384
	ds_read_b128 v[228:231], v204 offset:17408
	ds_read_b128 v[212:215], v204 offset:18432
	ds_read_b128 v[232:235], v204 offset:19456
	ds_read_b128 v[218:221], v204 offset:20480
	ds_read_b128 v[236:239], v204 offset:21504
	ds_read_b128 v[224:227], v204 offset:22528
	ds_read_b128 v[240:243], v204 offset:23552
	global_load_lds_dwordx4 v172, s[22:23]
	s_add_i32 m0, s64, 0x2000
	s_add_u32 s64, s22, 0x40000
	v_lshl_add_u64 v[186:187], s[22:23], 0, v[174:175]
	s_addc_u32 s65, s23, 0
	s_add_i32 s66, s43, s27
	global_load_lds_dwordx4 v174, s[22:23]
	s_mov_b32 m0, s66
	v_lshl_add_u64 v[188:189], s[24:25], 0, v[178:179]
	global_load_lds_dwordx4 v172, s[64:65]
	s_add_i32 m0, s66, 0x2000
	v_lshl_add_u64 v[190:191], s[24:25], 0, v[176:177]
	global_load_lds_dwordx4 v174, s[64:65]
	s_mov_b32 m0, s35
	s_nop 0
	global_load_lds_dwordx4 v178, s[24:25]
	s_mov_b32 m0, s36
	s_nop 0
	global_load_lds_dwordx4 v176, s[24:25]
	s_waitcnt vmcnt(8)
	s_waitcnt lgkmcnt(0)
	s_barrier
	s_setprio 1
	s_waitcnt lgkmcnt(0)
	v_mov_b32_e32 v210, v228
	v_mov_b32_e32 v211, v229
	s_nop 1
	v_mfma_scale_f32_16x16x128_f8f6f4 v[86:89], v[20:25], v[206:211], v[86:89], v168, v230 op_sel_hi:[0,0,0] cbsz:2 blgp:2
	v_mfma_scale_f32_16x16x128_f8f6f4 v[74:77], v[14:19], v[206:211], v[74:77], v164, v230 op_sel_hi:[0,0,0] cbsz:2 blgp:2
	v_mov_b32_e32 v216, v232
	v_mov_b32_e32 v217, v233
	s_nop 1
	v_mfma_scale_f32_16x16x128_f8f6f4 v[70:73], v[20:25], v[212:217], v[70:73], v168, v234 op_sel_hi:[0,0,0] cbsz:2 blgp:2
	v_mfma_scale_f32_16x16x128_f8f6f4 v[58:61], v[14:19], v[212:217], v[58:61], v164, v234 op_sel_hi:[0,0,0] cbsz:2 blgp:2
	v_mov_b32_e32 v222, v236
	v_mov_b32_e32 v223, v237
	s_nop 1
	v_mfma_scale_f32_16x16x128_f8f6f4 v[54:57], v[20:25], v[218:223], v[54:57], v168, v238 op_sel_hi:[0,0,0] cbsz:2 blgp:2
	v_mfma_scale_f32_16x16x128_f8f6f4 v[42:45], v[14:19], v[218:223], v[42:45], v164, v238 op_sel_hi:[0,0,0] cbsz:2 blgp:2
	v_mov_b32_e32 v228, v240
	v_mov_b32_e32 v229, v241
	s_nop 1
	v_mfma_scale_f32_16x16x128_f8f6f4 v[38:41], v[20:25], v[224:229], v[38:41], v168, v242 op_sel_hi:[0,0,0] cbsz:2 blgp:2
	v_mfma_scale_f32_16x16x128_f8f6f4 v[26:29], v[14:19], v[224:229], v[26:29], v164, v242 op_sel_hi:[0,0,0] cbsz:2 blgp:2
	s_setprio 0
	s_setprio 1
	v_mfma_scale_f32_16x16x128_f8f6f4 v[82:85], v[8:13], v[206:211], v[82:85], v160, v230 op_sel_hi:[0,0,0] cbsz:2 blgp:2
	v_mfma_scale_f32_16x16x128_f8f6f4 v[78:81], v[2:7], v[206:211], v[78:81], v156, v230 op_sel_hi:[0,0,0] cbsz:2 blgp:2
	v_mfma_scale_f32_16x16x128_f8f6f4 v[66:69], v[8:13], v[212:217], v[66:69], v160, v234 op_sel_hi:[0,0,0] cbsz:2 blgp:2
	v_mfma_scale_f32_16x16x128_f8f6f4 v[62:65], v[2:7], v[212:217], v[62:65], v156, v234 op_sel_hi:[0,0,0] cbsz:2 blgp:2
	v_mfma_scale_f32_16x16x128_f8f6f4 v[50:53], v[8:13], v[218:223], v[50:53], v160, v238 op_sel_hi:[0,0,0] cbsz:2 blgp:2
	v_mfma_scale_f32_16x16x128_f8f6f4 v[46:49], v[2:7], v[218:223], v[46:49], v156, v238 op_sel_hi:[0,0,0] cbsz:2 blgp:2
	v_mfma_scale_f32_16x16x128_f8f6f4 v[34:37], v[8:13], v[224:229], v[34:37], v160, v242 op_sel_hi:[0,0,0] cbsz:2 blgp:2
	v_mfma_scale_f32_16x16x128_f8f6f4 v[30:33], v[2:7], v[224:229], v[30:33], v156, v242 op_sel_hi:[0,0,0] cbsz:2 blgp:2
	s_setprio 0
	s_barrier
	s_add_i32 s64, 0, 0x18000
	s_add_i32 s65, 0, 0x1c000
	v_add_u32_e32 v2, s64, v198
	v_add_u32_e32 v6, s65, v198
	ds_read_b128 v[20:23], v2
	ds_read_b128 v[166:169], v2 offset:1024
	ds_read_b128 v[14:17], v2 offset:2048
	ds_read_b128 v[162:165], v2 offset:3072
	ds_read_b128 v[8:11], v6
	ds_read_b128 v[154:157], v6 offset:1024
	ds_read_b128 v[2:5], v6 offset:2048
	ds_read_b128 v[158:161], v6 offset:3072
	s_add_u32 s24, s24, 0x40000
	s_addc_u32 s25, s25, 0
	s_mov_b32 m0, s37
	ds_read_b128 v[206:209], v204 offset:32768
	ds_read_b128 v[228:231], v204 offset:33792
	ds_read_b128 v[212:215], v204 offset:34816
	ds_read_b128 v[232:235], v204 offset:35840
	ds_read_b128 v[218:221], v204 offset:36864
	ds_read_b128 v[236:239], v204 offset:37888
	ds_read_b128 v[224:227], v204 offset:38912
	ds_read_b128 v[240:243], v204 offset:39936
	global_load_lds_dwordx4 v178, s[24:25]
	s_mov_b32 m0, s38
	s_nop 0
	global_load_lds_dwordx4 v176, s[24:25]
	s_waitcnt vmcnt(8)
	s_waitcnt lgkmcnt(0)
	s_barrier
	s_setprio 1
	s_waitcnt lgkmcnt(0)
	v_mov_b32_e32 v24, v166
	v_mov_b32_e32 v25, v167
	v_mov_b32_e32 v210, v228
	v_mov_b32_e32 v211, v229
	s_nop 1
	v_mfma_scale_f32_16x16x128_f8f6f4 v[150:153], v[20:25], v[206:211], v[150:153], v168, v230 op_sel_hi:[0,0,0] cbsz:2 blgp:2
	v_mov_b32_e32 v18, v162
	v_mov_b32_e32 v19, v163
	s_nop 1
	v_mfma_scale_f32_16x16x128_f8f6f4 v[138:141], v[14:19], v[206:211], v[138:141], v164, v230 op_sel_hi:[0,0,0] cbsz:2 blgp:2
	v_mov_b32_e32 v216, v232
	v_mov_b32_e32 v217, v233
	s_nop 1
	v_mfma_scale_f32_16x16x128_f8f6f4 v[134:137], v[20:25], v[212:217], v[134:137], v168, v234 op_sel_hi:[0,0,0] cbsz:2 blgp:2
	v_mfma_scale_f32_16x16x128_f8f6f4 v[122:125], v[14:19], v[212:217], v[122:125], v164, v234 op_sel_hi:[0,0,0] cbsz:2 blgp:2
	v_mov_b32_e32 v222, v236
	v_mov_b32_e32 v223, v237
	s_nop 1
	v_mfma_scale_f32_16x16x128_f8f6f4 v[118:121], v[20:25], v[218:223], v[118:121], v168, v238 op_sel_hi:[0,0,0] cbsz:2 blgp:2
	v_mfma_scale_f32_16x16x128_f8f6f4 v[106:109], v[14:19], v[218:223], v[106:109], v164, v238 op_sel_hi:[0,0,0] cbsz:2 blgp:2
	v_mov_b32_e32 v228, v240
	v_mov_b32_e32 v229, v241
	s_nop 1
	v_mfma_scale_f32_16x16x128_f8f6f4 v[102:105], v[20:25], v[224:229], v[102:105], v168, v242 op_sel_hi:[0,0,0] cbsz:2 blgp:2
	v_mfma_scale_f32_16x16x128_f8f6f4 v[90:93], v[14:19], v[224:229], v[90:93], v164, v242 op_sel_hi:[0,0,0] cbsz:2 blgp:2
	s_setprio 0
	s_setprio 1
	v_mov_b32_e32 v12, v154
	v_mov_b32_e32 v13, v155
	s_nop 1
	v_mfma_scale_f32_16x16x128_f8f6f4 v[146:149], v[8:13], v[206:211], v[146:149], v156, v230 op_sel_hi:[0,0,0] cbsz:2 blgp:2
	v_mov_b32_e32 v6, v158
	v_mov_b32_e32 v7, v159
	s_nop 1
	v_mfma_scale_f32_16x16x128_f8f6f4 v[142:145], v[2:7], v[206:211], v[142:145], v160, v230 op_sel_hi:[0,0,0] cbsz:2 blgp:2
	v_mfma_scale_f32_16x16x128_f8f6f4 v[130:133], v[8:13], v[212:217], v[130:133], v156, v234 op_sel_hi:[0,0,0] cbsz:2 blgp:2
	v_mfma_scale_f32_16x16x128_f8f6f4 v[126:129], v[2:7], v[212:217], v[126:129], v160, v234 op_sel_hi:[0,0,0] cbsz:2 blgp:2
	v_mfma_scale_f32_16x16x128_f8f6f4 v[114:117], v[8:13], v[218:223], v[114:117], v156, v238 op_sel_hi:[0,0,0] cbsz:2 blgp:2
	v_mfma_scale_f32_16x16x128_f8f6f4 v[110:113], v[2:7], v[218:223], v[110:113], v160, v238 op_sel_hi:[0,0,0] cbsz:2 blgp:2
	v_mfma_scale_f32_16x16x128_f8f6f4 v[98:101], v[8:13], v[224:229], v[98:101], v156, v242 op_sel_hi:[0,0,0] cbsz:2 blgp:2
	v_mfma_scale_f32_16x16x128_f8f6f4 v[94:97], v[2:7], v[224:229], v[94:97], v160, v242 op_sel_hi:[0,0,0] cbsz:2 blgp:2
	s_setprio 0
	s_barrier
	s_add_i32 s24, s64, s27
	v_lshl_add_u64 v[154:155], v[184:185], 0, s[6:7]
	s_mov_b32 m0, s24
	ds_read_b128 v[206:209], v204 offset:49152
	ds_read_b128 v[228:231], v204 offset:50176
	ds_read_b128 v[212:215], v204 offset:51200
	ds_read_b128 v[232:235], v204 offset:52224
	ds_read_b128 v[218:221], v204 offset:53248
	ds_read_b128 v[236:239], v204 offset:54272
	ds_read_b128 v[224:227], v204 offset:55296
	ds_read_b128 v[240:243], v204 offset:56320
	global_load_lds_dwordx4 v[154:155], off
	s_add_i32 m0, s24, 0x2000
	s_add_u32 s22, s22, 0x40080
	v_lshl_add_u64 v[154:155], v[186:187], 0, s[6:7]
	s_addc_u32 s23, s23, 0
	s_add_i32 s24, s65, s27
	global_load_lds_dwordx4 v[154:155], off
	s_mov_b32 m0, s24
	s_nop 0
	global_load_lds_dwordx4 v172, s[22:23]
	s_add_i32 m0, s24, 0x2000
	s_nop 0
	global_load_lds_dwordx4 v174, s[22:23]
	v_lshl_add_u64 v[154:155], v[188:189], 0, s[6:7]
	s_mov_b32 m0, s39
	s_nop 0
	global_load_lds_dwordx4 v[154:155], off
	v_lshl_add_u64 v[154:155], v[190:191], 0, s[6:7]
	s_mov_b32 m0, s40
	s_nop 0
	global_load_lds_dwordx4 v[154:155], off
	s_waitcnt vmcnt(8)
	s_waitcnt lgkmcnt(0)
	s_barrier
	s_setprio 1
	s_waitcnt lgkmcnt(0)
	v_mov_b32_e32 v210, v228
	v_mov_b32_e32 v211, v229
	s_nop 1
	v_mfma_scale_f32_16x16x128_f8f6f4 v[86:89], v[20:25], v[206:211], v[86:89], v168, v230 op_sel_hi:[0,0,0] cbsz:2 blgp:2
	v_mfma_scale_f32_16x16x128_f8f6f4 v[74:77], v[14:19], v[206:211], v[74:77], v164, v230 op_sel_hi:[0,0,0] cbsz:2 blgp:2
	v_mov_b32_e32 v216, v232
	v_mov_b32_e32 v217, v233
	s_nop 1
	v_mfma_scale_f32_16x16x128_f8f6f4 v[70:73], v[20:25], v[212:217], v[70:73], v168, v234 op_sel_hi:[0,0,0] cbsz:2 blgp:2
	v_mfma_scale_f32_16x16x128_f8f6f4 v[58:61], v[14:19], v[212:217], v[58:61], v164, v234 op_sel_hi:[0,0,0] cbsz:2 blgp:2
	v_mov_b32_e32 v222, v236
	v_mov_b32_e32 v223, v237
	s_nop 1
	v_mfma_scale_f32_16x16x128_f8f6f4 v[54:57], v[20:25], v[218:223], v[54:57], v168, v238 op_sel_hi:[0,0,0] cbsz:2 blgp:2
	v_mfma_scale_f32_16x16x128_f8f6f4 v[42:45], v[14:19], v[218:223], v[42:45], v164, v238 op_sel_hi:[0,0,0] cbsz:2 blgp:2
	v_mov_b32_e32 v228, v240
	v_mov_b32_e32 v229, v241
	s_nop 1
	v_mfma_scale_f32_16x16x128_f8f6f4 v[38:41], v[20:25], v[224:229], v[38:41], v168, v242 op_sel_hi:[0,0,0] cbsz:2 blgp:2
	v_mfma_scale_f32_16x16x128_f8f6f4 v[26:29], v[14:19], v[224:229], v[26:29], v164, v242 op_sel_hi:[0,0,0] cbsz:2 blgp:2
	s_setprio 0
	s_setprio 1
	v_mfma_scale_f32_16x16x128_f8f6f4 v[82:85], v[8:13], v[206:211], v[82:85], v156, v230 op_sel_hi:[0,0,0] cbsz:2 blgp:2
	v_mfma_scale_f32_16x16x128_f8f6f4 v[78:81], v[2:7], v[206:211], v[78:81], v160, v230 op_sel_hi:[0,0,0] cbsz:2 blgp:2
	v_mfma_scale_f32_16x16x128_f8f6f4 v[66:69], v[8:13], v[212:217], v[66:69], v156, v234 op_sel_hi:[0,0,0] cbsz:2 blgp:2
	v_mfma_scale_f32_16x16x128_f8f6f4 v[62:65], v[2:7], v[212:217], v[62:65], v160, v234 op_sel_hi:[0,0,0] cbsz:2 blgp:2
	v_mfma_scale_f32_16x16x128_f8f6f4 v[50:53], v[8:13], v[218:223], v[50:53], v156, v238 op_sel_hi:[0,0,0] cbsz:2 blgp:2
	v_mfma_scale_f32_16x16x128_f8f6f4 v[46:49], v[2:7], v[218:223], v[46:49], v160, v238 op_sel_hi:[0,0,0] cbsz:2 blgp:2
	v_mfma_scale_f32_16x16x128_f8f6f4 v[34:37], v[8:13], v[224:229], v[34:37], v156, v242 op_sel_hi:[0,0,0] cbsz:2 blgp:2
	v_mfma_scale_f32_16x16x128_f8f6f4 v[30:33], v[2:7], v[224:229], v[30:33], v160, v242 op_sel_hi:[0,0,0] cbsz:2 blgp:2
	s_setprio 0
	s_barrier
	s_add_i32 s63, s63, 2
	s_add_u32 s20, s20, 0x100
	s_addc_u32 s21, s21, 0
	s_add_u32 s61, s61, 0x100
	s_addc_u32 s62, s62, 0
	s_cmp_gt_u32 s63, 13
	s_cbranch_scc0 .LBB0_1257
	s_and_b64 vcc, exec, s[8:9]
	s_cbranch_vccz .LBB0_1260
	s_barrier

.LBB0_1279:
	ds_read_b128 v[20:23], v195
	ds_read_b128 v[166:169], v195 offset:1024
	ds_read_b128 v[14:17], v195 offset:2048
	ds_read_b128 v[162:165], v195 offset:3072
	ds_read_b128 v[8:11], v196
	ds_read_b128 v[158:161], v196 offset:1024
	ds_read_b128 v[2:5], v196 offset:2048
	ds_read_b128 v[154:157], v196 offset:3072
	s_add_u32 s24, s22, 0xfffc0080
	s_addc_u32 s25, s23, -1
	s_cmp_eq_u32 s61, 12
	s_cselect_b32 s27, s11, s25
	s_cselect_b32 s26, s49, s24
	s_cselect_b32 s25, s13, s60
	s_cselect_b32 s24, s50, s51
	s_mov_b32 m0, s46
	ds_read_b128 v[184:187], v198
	ds_read_b128 v[188:191], v198 offset:1024
	ds_read_b128 v[202:205], v198 offset:2048
	ds_read_b128 v[218:221], v198 offset:3072
	ds_read_b128 v[208:211], v198 offset:4096
	ds_read_b128 v[222:225], v198 offset:5120
	ds_read_b128 v[214:217], v198 offset:6144
	ds_read_b128 v[226:229], v198 offset:7168
	global_load_lds_dwordx4 v180, s[22:23]
	s_add_i32 m0, s21, 0xe000
	s_nop 0
	global_load_lds_dwordx4 v182, s[22:23]
	s_waitcnt vmcnt(8)
	s_waitcnt lgkmcnt(0)
	s_barrier
	s_setprio 1
	s_waitcnt lgkmcnt(0)
	v_mov_b32_e32 v24, v166
	v_mov_b32_e32 v25, v167
	s_nop 1
	v_mfma_scale_f32_16x16x128_f8f6f4 v[150:153], v[20:25], v[184:189], v[150:153], v168, v190 op_sel_hi:[0,0,0] cbsz:2 blgp:2
	v_mov_b32_e32 v18, v162
	v_mov_b32_e32 v19, v163
	s_nop 1
	v_mfma_scale_f32_16x16x128_f8f6f4 v[138:141], v[14:19], v[184:189], v[138:141], v164, v190 op_sel_hi:[0,0,0] cbsz:2 blgp:2
	v_mov_b32_e32 v206, v218
	v_mov_b32_e32 v207, v219
	s_nop 1
	v_mfma_scale_f32_16x16x128_f8f6f4 v[134:137], v[20:25], v[202:207], v[134:137], v168, v220 op_sel_hi:[0,0,0] cbsz:2 blgp:2
	v_mfma_scale_f32_16x16x128_f8f6f4 v[122:125], v[14:19], v[202:207], v[122:125], v164, v220 op_sel_hi:[0,0,0] cbsz:2 blgp:2
	v_mov_b32_e32 v212, v222
	v_mov_b32_e32 v213, v223
	s_nop 1
	v_mfma_scale_f32_16x16x128_f8f6f4 v[118:121], v[20:25], v[208:213], v[118:121], v168, v224 op_sel_hi:[0,0,0] cbsz:2 blgp:2
	v_mfma_scale_f32_16x16x128_f8f6f4 v[106:109], v[14:19], v[208:213], v[106:109], v164, v224 op_sel_hi:[0,0,0] cbsz:2 blgp:2
	v_mov_b32_e32 v218, v226
	v_mov_b32_e32 v219, v227
	s_nop 1
	v_mfma_scale_f32_16x16x128_f8f6f4 v[102:105], v[20:25], v[214:219], v[102:105], v168, v228 op_sel_hi:[0,0,0] cbsz:2 blgp:2
	v_mfma_scale_f32_16x16x128_f8f6f4 v[90:93], v[14:19], v[214:219], v[90:93], v164, v228 op_sel_hi:[0,0,0] cbsz:2 blgp:2
	s_setprio 0
	s_setprio 1
	v_mov_b32_e32 v12, v158
	v_mov_b32_e32 v13, v159
	s_nop 1
	v_mfma_scale_f32_16x16x128_f8f6f4 v[146:149], v[8:13], v[184:189], v[146:149], v160, v190 op_sel_hi:[0,0,0] cbsz:2 blgp:2
	v_mov_b32_e32 v6, v154
	v_mov_b32_e32 v7, v155
	s_nop 1
	v_mfma_scale_f32_16x16x128_f8f6f4 v[142:145], v[2:7], v[184:189], v[142:145], v156, v190 op_sel_hi:[0,0,0] cbsz:2 blgp:2
	v_mfma_scale_f32_16x16x128_f8f6f4 v[130:133], v[8:13], v[202:207], v[130:133], v160, v220 op_sel_hi:[0,0,0] cbsz:2 blgp:2
	v_mfma_scale_f32_16x16x128_f8f6f4 v[126:129], v[2:7], v[202:207], v[126:129], v156, v220 op_sel_hi:[0,0,0] cbsz:2 blgp:2
	v_mfma_scale_f32_16x16x128_f8f6f4 v[114:117], v[8:13], v[208:213], v[114:117], v160, v224 op_sel_hi:[0,0,0] cbsz:2 blgp:2
	v_mfma_scale_f32_16x16x128_f8f6f4 v[110:113], v[2:7], v[208:213], v[110:113], v156, v224 op_sel_hi:[0,0,0] cbsz:2 blgp:2
	v_mfma_scale_f32_16x16x128_f8f6f4 v[98:101], v[8:13], v[214:219], v[98:101], v160, v228 op_sel_hi:[0,0,0] cbsz:2 blgp:2
	v_mfma_scale_f32_16x16x128_f8f6f4 v[94:97], v[2:7], v[214:219], v[94:97], v156, v228 op_sel_hi:[0,0,0] cbsz:2 blgp:2
	s_setprio 0
	s_barrier
	s_add_i32 s62, s42, s35
	v_lshl_add_u64 v[184:185], s[24:25], 0, v[176:177]
	s_mov_b32 m0, s62
	ds_read_b128 v[202:205], v198 offset:16384
	ds_read_b128 v[224:227], v198 offset:17408
	ds_read_b128 v[208:211], v198 offset:18432
	ds_read_b128 v[228:231], v198 offset:19456
	ds_read_b128 v[214:217], v198 offset:20480
	ds_read_b128 v[232:235], v198 offset:21504
	ds_read_b128 v[220:223], v198 offset:22528
	ds_read_b128 v[236:239], v198 offset:23552
	global_load_lds_dwordx4 v176, s[24:25]
	s_add_i32 m0, s62, 0x2000
	s_add_u32 s62, s24, 0x40000
	v_lshl_add_u64 v[186:187], s[24:25], 0, v[172:173]
	s_addc_u32 s63, s25, 0
	s_add_i32 s64, s43, s35
	global_load_lds_dwordx4 v172, s[24:25]
	s_mov_b32 m0, s64
	v_lshl_add_u64 v[188:189], s[26:27], 0, v[178:179]
	global_load_lds_dwordx4 v176, s[62:63]
	s_add_i32 m0, s64, 0x2000
	v_lshl_add_u64 v[190:191], s[26:27], 0, v[174:175]
	global_load_lds_dwordx4 v172, s[62:63]
	s_mov_b32 m0, s21
	s_nop 0
	global_load_lds_dwordx4 v178, s[26:27]
	s_mov_b32 m0, s36
	s_nop 0
	global_load_lds_dwordx4 v174, s[26:27]
	s_waitcnt vmcnt(8)
	s_waitcnt lgkmcnt(0)
	s_barrier
	s_setprio 1
	s_waitcnt lgkmcnt(0)
	v_mov_b32_e32 v206, v224
	v_mov_b32_e32 v207, v225
	s_nop 1
	v_mfma_scale_f32_16x16x128_f8f6f4 v[86:89], v[20:25], v[202:207], v[86:89], v168, v226 op_sel_hi:[0,0,0] cbsz:2 blgp:2
	v_mfma_scale_f32_16x16x128_f8f6f4 v[74:77], v[14:19], v[202:207], v[74:77], v164, v226 op_sel_hi:[0,0,0] cbsz:2 blgp:2
	v_mov_b32_e32 v212, v228
	v_mov_b32_e32 v213, v229
	s_nop 1
	v_mfma_scale_f32_16x16x128_f8f6f4 v[70:73], v[20:25], v[208:213], v[70:73], v168, v230 op_sel_hi:[0,0,0] cbsz:2 blgp:2
	v_mfma_scale_f32_16x16x128_f8f6f4 v[58:61], v[14:19], v[208:213], v[58:61], v164, v230 op_sel_hi:[0,0,0] cbsz:2 blgp:2
	v_mov_b32_e32 v218, v232
	v_mov_b32_e32 v219, v233
	s_nop 1
	v_mfma_scale_f32_16x16x128_f8f6f4 v[54:57], v[20:25], v[214:219], v[54:57], v168, v234 op_sel_hi:[0,0,0] cbsz:2 blgp:2
	v_mfma_scale_f32_16x16x128_f8f6f4 v[42:45], v[14:19], v[214:219], v[42:45], v164, v234 op_sel_hi:[0,0,0] cbsz:2 blgp:2
	v_mov_b32_e32 v224, v236
	v_mov_b32_e32 v225, v237
	s_nop 1
	v_mfma_scale_f32_16x16x128_f8f6f4 v[38:41], v[20:25], v[220:225], v[38:41], v168, v238 op_sel_hi:[0,0,0] cbsz:2 blgp:2
	v_mfma_scale_f32_16x16x128_f8f6f4 v[26:29], v[14:19], v[220:225], v[26:29], v164, v238 op_sel_hi:[0,0,0] cbsz:2 blgp:2
	s_setprio 0
	s_setprio 1
	v_mfma_scale_f32_16x16x128_f8f6f4 v[82:85], v[8:13], v[202:207], v[82:85], v160, v226 op_sel_hi:[0,0,0] cbsz:2 blgp:2
	v_mfma_scale_f32_16x16x128_f8f6f4 v[78:81], v[2:7], v[202:207], v[78:81], v156, v226 op_sel_hi:[0,0,0] cbsz:2 blgp:2
	v_mfma_scale_f32_16x16x128_f8f6f4 v[66:69], v[8:13], v[208:213], v[66:69], v160, v230 op_sel_hi:[0,0,0] cbsz:2 blgp:2
	v_mfma_scale_f32_16x16x128_f8f6f4 v[62:65], v[2:7], v[208:213], v[62:65], v156, v230 op_sel_hi:[0,0,0] cbsz:2 blgp:2
	v_mfma_scale_f32_16x16x128_f8f6f4 v[50:53], v[8:13], v[214:219], v[50:53], v160, v234 op_sel_hi:[0,0,0] cbsz:2 blgp:2
	v_mfma_scale_f32_16x16x128_f8f6f4 v[46:49], v[2:7], v[214:219], v[46:49], v156, v234 op_sel_hi:[0,0,0] cbsz:2 blgp:2
	v_mfma_scale_f32_16x16x128_f8f6f4 v[34:37], v[8:13], v[220:225], v[34:37], v160, v238 op_sel_hi:[0,0,0] cbsz:2 blgp:2
	v_mfma_scale_f32_16x16x128_f8f6f4 v[30:33], v[2:7], v[220:225], v[30:33], v156, v238 op_sel_hi:[0,0,0] cbsz:2 blgp:2
	s_setprio 0
	s_barrier
	s_add_i32 s62, 0, 0x18000
	s_add_i32 s63, 0, 0x1c000
	v_add_u32_e32 v2, s62, v194
	v_add_u32_e32 v6, s63, v194
	ds_read_b128 v[20:23], v2
	ds_read_b128 v[166:169], v2 offset:1024
	ds_read_b128 v[14:17], v2 offset:2048
	ds_read_b128 v[162:165], v2 offset:3072
	ds_read_b128 v[8:11], v6
	ds_read_b128 v[154:157], v6 offset:1024
	ds_read_b128 v[2:5], v6 offset:2048
	ds_read_b128 v[158:161], v6 offset:3072
	s_add_u32 s26, s26, 0x40000
	s_addc_u32 s27, s27, 0
	s_mov_b32 m0, s37
	ds_read_b128 v[202:205], v198 offset:32768
	ds_read_b128 v[224:227], v198 offset:33792
	ds_read_b128 v[208:211], v198 offset:34816
	ds_read_b128 v[228:231], v198 offset:35840
	ds_read_b128 v[214:217], v198 offset:36864
	ds_read_b128 v[232:235], v198 offset:37888
	ds_read_b128 v[220:223], v198 offset:38912
	ds_read_b128 v[236:239], v198 offset:39936
	global_load_lds_dwordx4 v178, s[26:27]
	s_mov_b32 m0, s38
	s_nop 0
	global_load_lds_dwordx4 v174, s[26:27]
	s_waitcnt vmcnt(8)
	s_waitcnt lgkmcnt(0)
	s_barrier
	s_setprio 1
	s_waitcnt lgkmcnt(0)
	v_mov_b32_e32 v24, v166
	v_mov_b32_e32 v25, v167
	v_mov_b32_e32 v206, v224
	v_mov_b32_e32 v207, v225
	s_nop 1
	v_mfma_scale_f32_16x16x128_f8f6f4 v[150:153], v[20:25], v[202:207], v[150:153], v168, v226 op_sel_hi:[0,0,0] cbsz:2 blgp:2
	v_mov_b32_e32 v18, v162
	v_mov_b32_e32 v19, v163
	s_nop 1
	v_mfma_scale_f32_16x16x128_f8f6f4 v[138:141], v[14:19], v[202:207], v[138:141], v164, v226 op_sel_hi:[0,0,0] cbsz:2 blgp:2
	v_mov_b32_e32 v212, v228
	v_mov_b32_e32 v213, v229
	s_nop 1
	v_mfma_scale_f32_16x16x128_f8f6f4 v[134:137], v[20:25], v[208:213], v[134:137], v168, v230 op_sel_hi:[0,0,0] cbsz:2 blgp:2
	v_mfma_scale_f32_16x16x128_f8f6f4 v[122:125], v[14:19], v[208:213], v[122:125], v164, v230 op_sel_hi:[0,0,0] cbsz:2 blgp:2
	v_mov_b32_e32 v218, v232
	v_mov_b32_e32 v219, v233
	s_nop 1
	v_mfma_scale_f32_16x16x128_f8f6f4 v[118:121], v[20:25], v[214:219], v[118:121], v168, v234 op_sel_hi:[0,0,0] cbsz:2 blgp:2
	v_mfma_scale_f32_16x16x128_f8f6f4 v[106:109], v[14:19], v[214:219], v[106:109], v164, v234 op_sel_hi:[0,0,0] cbsz:2 blgp:2
	v_mov_b32_e32 v224, v236
	v_mov_b32_e32 v225, v237
	s_nop 1
	v_mfma_scale_f32_16x16x128_f8f6f4 v[102:105], v[20:25], v[220:225], v[102:105], v168, v238 op_sel_hi:[0,0,0] cbsz:2 blgp:2
	v_mfma_scale_f32_16x16x128_f8f6f4 v[90:93], v[14:19], v[220:225], v[90:93], v164, v238 op_sel_hi:[0,0,0] cbsz:2 blgp:2
	s_setprio 0
	s_setprio 1
	v_mov_b32_e32 v12, v154
	v_mov_b32_e32 v13, v155
	s_nop 1
	v_mfma_scale_f32_16x16x128_f8f6f4 v[146:149], v[8:13], v[202:207], v[146:149], v156, v226 op_sel_hi:[0,0,0] cbsz:2 blgp:2
	v_mov_b32_e32 v6, v158
	v_mov_b32_e32 v7, v159
	s_nop 1
	v_mfma_scale_f32_16x16x128_f8f6f4 v[142:145], v[2:7], v[202:207], v[142:145], v160, v226 op_sel_hi:[0,0,0] cbsz:2 blgp:2
	v_mfma_scale_f32_16x16x128_f8f6f4 v[130:133], v[8:13], v[208:213], v[130:133], v156, v230 op_sel_hi:[0,0,0] cbsz:2 blgp:2
	v_mfma_scale_f32_16x16x128_f8f6f4 v[126:129], v[2:7], v[208:213], v[126:129], v160, v230 op_sel_hi:[0,0,0] cbsz:2 blgp:2
	v_mfma_scale_f32_16x16x128_f8f6f4 v[114:117], v[8:13], v[214:219], v[114:117], v156, v234 op_sel_hi:[0,0,0] cbsz:2 blgp:2
	v_mfma_scale_f32_16x16x128_f8f6f4 v[110:113], v[2:7], v[214:219], v[110:113], v160, v234 op_sel_hi:[0,0,0] cbsz:2 blgp:2
	v_mfma_scale_f32_16x16x128_f8f6f4 v[98:101], v[8:13], v[220:225], v[98:101], v156, v238 op_sel_hi:[0,0,0] cbsz:2 blgp:2
	v_mfma_scale_f32_16x16x128_f8f6f4 v[94:97], v[2:7], v[220:225], v[94:97], v160, v238 op_sel_hi:[0,0,0] cbsz:2 blgp:2
	s_setprio 0
	s_barrier
	s_add_i32 s26, s62, s35
	v_lshl_add_u64 v[154:155], v[184:185], 0, s[6:7]
	s_mov_b32 m0, s26
	ds_read_b128 v[202:205], v198 offset:49152
	ds_read_b128 v[224:227], v198 offset:50176
	ds_read_b128 v[208:211], v198 offset:51200
	ds_read_b128 v[228:231], v198 offset:52224
	ds_read_b128 v[214:217], v198 offset:53248
	ds_read_b128 v[232:235], v198 offset:54272
	ds_read_b128 v[220:223], v198 offset:55296
	ds_read_b128 v[236:239], v198 offset:56320
	global_load_lds_dwordx4 v[154:155], off
	s_add_i32 m0, s26, 0x2000
	s_add_u32 s24, s24, 0x40080
	v_lshl_add_u64 v[154:155], v[186:187], 0, s[6:7]
	s_addc_u32 s25, s25, 0
	s_add_i32 s26, s63, s35
	global_load_lds_dwordx4 v[154:155], off
	s_mov_b32 m0, s26
	s_nop 0
	global_load_lds_dwordx4 v176, s[24:25]
	s_add_i32 m0, s26, 0x2000
	s_nop 0
	global_load_lds_dwordx4 v172, s[24:25]
	v_lshl_add_u64 v[154:155], v[188:189], 0, s[6:7]
	s_mov_b32 m0, s40
	s_nop 0
	global_load_lds_dwordx4 v[154:155], off
	v_lshl_add_u64 v[154:155], v[190:191], 0, s[6:7]
	s_mov_b32 m0, s41
	s_nop 0
	global_load_lds_dwordx4 v[154:155], off
	s_waitcnt vmcnt(8)
	s_waitcnt lgkmcnt(0)
	s_barrier
	s_setprio 1
	s_waitcnt lgkmcnt(0)
	v_mov_b32_e32 v206, v224
	v_mov_b32_e32 v207, v225
	s_nop 1
	v_mfma_scale_f32_16x16x128_f8f6f4 v[86:89], v[20:25], v[202:207], v[86:89], v168, v226 op_sel_hi:[0,0,0] cbsz:2 blgp:2
	v_mfma_scale_f32_16x16x128_f8f6f4 v[74:77], v[14:19], v[202:207], v[74:77], v164, v226 op_sel_hi:[0,0,0] cbsz:2 blgp:2
	v_mov_b32_e32 v212, v228
	v_mov_b32_e32 v213, v229
	s_nop 1
	v_mfma_scale_f32_16x16x128_f8f6f4 v[70:73], v[20:25], v[208:213], v[70:73], v168, v230 op_sel_hi:[0,0,0] cbsz:2 blgp:2
	v_mfma_scale_f32_16x16x128_f8f6f4 v[58:61], v[14:19], v[208:213], v[58:61], v164, v230 op_sel_hi:[0,0,0] cbsz:2 blgp:2
	v_mov_b32_e32 v218, v232
	v_mov_b32_e32 v219, v233
	s_nop 1
	v_mfma_scale_f32_16x16x128_f8f6f4 v[54:57], v[20:25], v[214:219], v[54:57], v168, v234 op_sel_hi:[0,0,0] cbsz:2 blgp:2
	v_mfma_scale_f32_16x16x128_f8f6f4 v[42:45], v[14:19], v[214:219], v[42:45], v164, v234 op_sel_hi:[0,0,0] cbsz:2 blgp:2
	v_mov_b32_e32 v224, v236
	v_mov_b32_e32 v225, v237
	s_nop 1
	v_mfma_scale_f32_16x16x128_f8f6f4 v[38:41], v[20:25], v[220:225], v[38:41], v168, v238 op_sel_hi:[0,0,0] cbsz:2 blgp:2
	v_mfma_scale_f32_16x16x128_f8f6f4 v[26:29], v[14:19], v[220:225], v[26:29], v164, v238 op_sel_hi:[0,0,0] cbsz:2 blgp:2
	s_setprio 0
	s_setprio 1
	v_mfma_scale_f32_16x16x128_f8f6f4 v[82:85], v[8:13], v[202:207], v[82:85], v156, v226 op_sel_hi:[0,0,0] cbsz:2 blgp:2
	v_mfma_scale_f32_16x16x128_f8f6f4 v[78:81], v[2:7], v[202:207], v[78:81], v160, v226 op_sel_hi:[0,0,0] cbsz:2 blgp:2
	v_mfma_scale_f32_16x16x128_f8f6f4 v[66:69], v[8:13], v[208:213], v[66:69], v156, v230 op_sel_hi:[0,0,0] cbsz:2 blgp:2
	v_mfma_scale_f32_16x16x128_f8f6f4 v[62:65], v[2:7], v[208:213], v[62:65], v160, v230 op_sel_hi:[0,0,0] cbsz:2 blgp:2
	v_mfma_scale_f32_16x16x128_f8f6f4 v[50:53], v[8:13], v[214:219], v[50:53], v156, v234 op_sel_hi:[0,0,0] cbsz:2 blgp:2
	v_mfma_scale_f32_16x16x128_f8f6f4 v[46:49], v[2:7], v[214:219], v[46:49], v160, v234 op_sel_hi:[0,0,0] cbsz:2 blgp:2
	v_mfma_scale_f32_16x16x128_f8f6f4 v[34:37], v[8:13], v[220:225], v[34:37], v156, v238 op_sel_hi:[0,0,0] cbsz:2 blgp:2
	v_mfma_scale_f32_16x16x128_f8f6f4 v[30:33], v[2:7], v[220:225], v[30:33], v160, v238 op_sel_hi:[0,0,0] cbsz:2 blgp:2
	s_setprio 0
	s_barrier
	s_add_i32 s61, s61, 2
	s_add_u32 s22, s22, 0x100
	s_addc_u32 s23, s23, 0
	s_add_u32 s51, s51, 0x100
	s_addc_u32 s60, s60, 0
	s_cmp_gt_u32 s61, 13
	s_cbranch_scc0 .LBB0_1279
	s_and_b64 vcc, exec, s[8:9]
	s_cbranch_vccz .LBB0_1282
	s_barrier
